# batch6: + P9 SwiGLU epilogue trimmed (merged exp-argument multiply, +1 folded into bias), P5 and P2 next-head conv tiles hand-scheduled with fma chains
# baseline (speedup 1.0000x reference)
.LBB0_402:
	s_or_b64 exec, exec, s[42:43]
	s_waitcnt vmcnt(4)
	v_cndmask_b32_e64 v18, v18, 0, s[12:13]
	v_cndmask_b32_e64 v19, v19, 0, s[12:13]
	v_cndmask_b32_e64 v20, v20, 0, s[12:13]
	v_lshlrev_b32_e32 v120, 16, v18
	v_and_b32_e32 v131, 0xffff0000, v18
	v_lshlrev_b32_e32 v121, 16, v19
	v_and_b32_e32 v132, 0xffff0000, v19
	v_lshlrev_b32_e32 v122, 16, v20
	v_and_b32_e32 v133, 0xffff0000, v20
	v_lshlrev_b32_e32 v123, 16, v116
	v_and_b32_e32 v134, 0xffff0000, v116
	v_lshlrev_b32_e32 v124, 16, v117
	v_and_b32_e32 v135, 0xffff0000, v117
	v_lshlrev_b32_e32 v125, 16, v118
	v_and_b32_e32 v136, 0xffff0000, v118
	v_lshlrev_b32_e32 v126, 16, v114
	v_and_b32_e32 v137, 0xffff0000, v114
	v_lshlrev_b32_e32 v127, 16, v115
	v_and_b32_e32 v138, 0xffff0000, v115
	v_lshlrev_b32_e32 v128, 16, v112
	v_and_b32_e32 v139, 0xffff0000, v112
	v_lshlrev_b32_e32 v129, 16, v113
	v_and_b32_e32 v140, 0xffff0000, v113
	v_lshlrev_b32_e32 v130, 16, v29
	v_and_b32_e32 v141, 0xffff0000, v29
	v_mov_b32_e32 v119, s26
	ds_read_b32 v29, v119 offset:5116
	v_add_u32_e32 v112, s26, v87
	ds_read2st64_b32 v[142:143], v112 offset0:2 offset1:18
	v_add_u32_e32 v119, s26, v104
	ds_read_b128 v[144:147], v119 offset:512
	ds_read_b128 v[112:115], v119 offset:4608
	ds_read_b96 v[116:118], v119 offset:528
	ds_read_b96 v[18:20], v119 offset:4624
	s_waitcnt lgkmcnt(0)
	v_sub_f32_e32 v112, v29, v112
	v_sub_f32_e32 v113, v29, v113
	v_sub_f32_e32 v114, v29, v114
	v_sub_f32_e32 v115, v29, v115
	v_sub_f32_e32 v18, v29, v18
	v_sub_f32_e32 v19, v29, v19
	v_sub_f32_e32 v20, v29, v20
	v_sub_f32_e32 v143, v29, v143
	v_mul_f32_e32 v112, 0x3fb8aa3b, v112
	v_mul_f32_e32 v113, 0x3fb8aa3b, v113
	v_mul_f32_e32 v114, 0x3fb8aa3b, v114
	v_mul_f32_e32 v115, 0x3fb8aa3b, v115
	v_mul_f32_e32 v18, 0x3fb8aa3b, v18
	v_mul_f32_e32 v19, 0x3fb8aa3b, v19
	v_mul_f32_e32 v20, 0x3fb8aa3b, v20
	v_mul_f32_e32 v143, 0x3fb8aa3b, v143
	v_exp_f32_e32 v112, v112
	v_exp_f32_e32 v113, v113
	v_exp_f32_e32 v114, v114
	v_exp_f32_e32 v115, v115
	v_exp_f32_e32 v18, v18
	v_exp_f32_e32 v19, v19
	v_exp_f32_e32 v20, v20
	v_exp_f32_e32 v143, v143
	v_mul_f32_e32 v144, v144, v112
	v_mul_f32_e32 v145, v145, v113
	v_mul_f32_e32 v146, v146, v114
	v_mul_f32_e32 v147, v147, v115
	v_mul_f32_e32 v116, v116, v18
	v_mul_f32_e32 v117, v117, v19
	v_mul_f32_e32 v118, v118, v20
	v_mul_f32_e32 v142, v142, v143
	v_fma_f32 v112, v48, v120, v50
	v_fma_f32 v113, v49, v131, v51
	v_fmac_f32_e32 v112, v56, v121
	v_fmac_f32_e32 v113, v57, v132
	v_fmac_f32_e32 v112, v46, v122
	v_fmac_f32_e32 v113, v47, v133
	v_fmac_f32_e32 v112, v54, v123
	v_fmac_f32_e32 v113, v55, v134
	v_mul_f32_e32 v114, 0xbfb8aa3b, v112
	v_mul_f32_e32 v115, 0xbfb8aa3b, v113
	v_exp_f32_e32 v114, v114
	v_exp_f32_e32 v115, v115
	v_add_f32_e32 v114, 1.0, v114
	v_add_f32_e32 v115, 1.0, v115
	v_rcp_f32_e32 v114, v114
	v_rcp_f32_e32 v115, v115
	v_mul_f32_e32 v112, v112, v144
	v_mul_f32_e32 v113, v113, v144
	v_mul_f32_e32 v120, v112, v114
	v_mul_f32_e32 v131, v113, v115
	v_fma_f32 v112, v48, v121, v50
	v_fma_f32 v113, v49, v132, v51
	v_fmac_f32_e32 v112, v56, v122
	v_fmac_f32_e32 v113, v57, v133
	v_fmac_f32_e32 v112, v46, v123
	v_fmac_f32_e32 v113, v47, v134
	v_fmac_f32_e32 v112, v54, v124
	v_fmac_f32_e32 v113, v55, v135
	v_mul_f32_e32 v114, 0xbfb8aa3b, v112
	v_mul_f32_e32 v115, 0xbfb8aa3b, v113
	v_exp_f32_e32 v114, v114
	v_exp_f32_e32 v115, v115
	v_add_f32_e32 v114, 1.0, v114
	v_add_f32_e32 v115, 1.0, v115
	v_rcp_f32_e32 v114, v114
	v_rcp_f32_e32 v115, v115
	v_mul_f32_e32 v112, v112, v145
	v_mul_f32_e32 v113, v113, v145
	v_mul_f32_e32 v121, v112, v114
	v_mul_f32_e32 v132, v113, v115
	v_fma_f32 v112, v48, v122, v50
	v_fma_f32 v113, v49, v133, v51
	v_fmac_f32_e32 v112, v56, v123
	v_fmac_f32_e32 v113, v57, v134
	v_fmac_f32_e32 v112, v46, v124
	v_fmac_f32_e32 v113, v47, v135
	v_fmac_f32_e32 v112, v54, v125
	v_fmac_f32_e32 v113, v55, v136
	v_mul_f32_e32 v114, 0xbfb8aa3b, v112
	v_mul_f32_e32 v115, 0xbfb8aa3b, v113
	v_exp_f32_e32 v114, v114
	v_exp_f32_e32 v115, v115
	v_add_f32_e32 v114, 1.0, v114
	v_add_f32_e32 v115, 1.0, v115
	v_rcp_f32_e32 v114, v114
	v_rcp_f32_e32 v115, v115
	v_mul_f32_e32 v112, v112, v146
	v_mul_f32_e32 v113, v113, v146
	v_mul_f32_e32 v122, v112, v114
	v_mul_f32_e32 v133, v113, v115
	v_fma_f32 v112, v48, v123, v50
	v_fma_f32 v113, v49, v134, v51
	v_fmac_f32_e32 v112, v56, v124
	v_fmac_f32_e32 v113, v57, v135
	v_fmac_f32_e32 v112, v46, v125
	v_fmac_f32_e32 v113, v47, v136
	v_fmac_f32_e32 v112, v54, v126
	v_fmac_f32_e32 v113, v55, v137
	v_mul_f32_e32 v114, 0xbfb8aa3b, v112
	v_mul_f32_e32 v115, 0xbfb8aa3b, v113
	v_exp_f32_e32 v114, v114
	v_exp_f32_e32 v115, v115
	v_add_f32_e32 v114, 1.0, v114
	v_add_f32_e32 v115, 1.0, v115
	v_rcp_f32_e32 v114, v114
	v_rcp_f32_e32 v115, v115
	v_mul_f32_e32 v112, v112, v147
	v_mul_f32_e32 v113, v113, v147
	v_mul_f32_e32 v123, v112, v114
	v_mul_f32_e32 v134, v113, v115
	v_fma_f32 v112, v48, v124, v50
	v_fma_f32 v113, v49, v135, v51
	v_fmac_f32_e32 v112, v56, v125
	v_fmac_f32_e32 v113, v57, v136
	v_fmac_f32_e32 v112, v46, v126
	v_fmac_f32_e32 v113, v47, v137
	v_fmac_f32_e32 v112, v54, v127
	v_fmac_f32_e32 v113, v55, v138
	v_mul_f32_e32 v114, 0xbfb8aa3b, v112
	v_mul_f32_e32 v115, 0xbfb8aa3b, v113
	v_exp_f32_e32 v114, v114
	v_exp_f32_e32 v115, v115
	v_add_f32_e32 v114, 1.0, v114
	v_add_f32_e32 v115, 1.0, v115
	v_rcp_f32_e32 v114, v114
	v_rcp_f32_e32 v115, v115
	v_mul_f32_e32 v112, v112, v116
	v_mul_f32_e32 v113, v113, v116
	v_mul_f32_e32 v124, v112, v114
	v_mul_f32_e32 v135, v113, v115
	v_fma_f32 v112, v48, v125, v50
	v_fma_f32 v113, v49, v136, v51
	v_fmac_f32_e32 v112, v56, v126
	v_fmac_f32_e32 v113, v57, v137
	v_fmac_f32_e32 v112, v46, v127
	v_fmac_f32_e32 v113, v47, v138
	v_fmac_f32_e32 v112, v54, v128
	v_fmac_f32_e32 v113, v55, v139
	v_mul_f32_e32 v114, 0xbfb8aa3b, v112
	v_mul_f32_e32 v115, 0xbfb8aa3b, v113
	v_exp_f32_e32 v114, v114
	v_exp_f32_e32 v115, v115
	v_add_f32_e32 v114, 1.0, v114
	v_add_f32_e32 v115, 1.0, v115
	v_rcp_f32_e32 v114, v114
	v_rcp_f32_e32 v115, v115
	v_mul_f32_e32 v112, v112, v117
	v_mul_f32_e32 v113, v113, v117
	v_mul_f32_e32 v125, v112, v114
	v_mul_f32_e32 v136, v113, v115
	v_fma_f32 v112, v48, v126, v50
	v_fma_f32 v113, v49, v137, v51
	v_fmac_f32_e32 v112, v56, v127
	v_fmac_f32_e32 v113, v57, v138
	v_fmac_f32_e32 v112, v46, v128
	v_fmac_f32_e32 v113, v47, v139
	v_fmac_f32_e32 v112, v54, v129
	v_fmac_f32_e32 v113, v55, v140
	v_mul_f32_e32 v114, 0xbfb8aa3b, v112
	v_mul_f32_e32 v115, 0xbfb8aa3b, v113
	v_exp_f32_e32 v114, v114
	v_exp_f32_e32 v115, v115
	v_add_f32_e32 v114, 1.0, v114
	v_add_f32_e32 v115, 1.0, v115
	v_rcp_f32_e32 v114, v114
	v_rcp_f32_e32 v115, v115
	v_mul_f32_e32 v112, v112, v118
	v_mul_f32_e32 v113, v113, v118
	v_mul_f32_e32 v126, v112, v114
	v_mul_f32_e32 v137, v113, v115
	v_fma_f32 v112, v48, v127, v50
	v_fma_f32 v113, v49, v138, v51
	v_fmac_f32_e32 v112, v56, v128
	v_fmac_f32_e32 v113, v57, v139
	v_fmac_f32_e32 v112, v46, v129
	v_fmac_f32_e32 v113, v47, v140
	v_fmac_f32_e32 v112, v54, v130
	v_fmac_f32_e32 v113, v55, v141
	v_mul_f32_e32 v114, 0xbfb8aa3b, v112
	v_mul_f32_e32 v115, 0xbfb8aa3b, v113
	v_exp_f32_e32 v114, v114
	v_exp_f32_e32 v115, v115
	v_add_f32_e32 v114, 1.0, v114
	v_add_f32_e32 v115, 1.0, v115
	v_rcp_f32_e32 v114, v114
	v_rcp_f32_e32 v115, v115
	v_mul_f32_e32 v112, v112, v142
	v_mul_f32_e32 v113, v113, v142
	v_mul_f32_e32 v127, v112, v114
	v_mul_f32_e32 v138, v113, v115
	s_and_b64 s[40:41], s[40:41], exec
	s_mov_b32 s40, 0xec00
	s_cselect_b32 s40, s40, 0xa800
	s_add_i32 s40, s40, 0
	s_add_i32 s62, s62, 1
	s_add_u32 s38, s38, 0x100
	s_addc_u32 s39, s39, 0
	s_addk_i32 s26, 0x200
	s_add_u32 s58, s58, 4
	s_addc_u32 s61, s61, 0
	v_cvt_pk_bf16_f32 v46, v120, v121
	v_cvt_pk_bf16_f32 v47, v122, v123
	v_cvt_pk_bf16_f32 v48, v124, v125
	v_cvt_pk_bf16_f32 v49, v126, v127
	v_cvt_pk_bf16_f32 v50, v131, v132
	v_cvt_pk_bf16_f32 v51, v133, v134
	v_cvt_pk_bf16_f32 v52, v135, v136
	v_cvt_pk_bf16_f32 v53, v137, v138
	v_add3_u32 v18, s40, v89, v90
	s_mov_b64 s[40:41], 0x4000
	v_lshl_add_u64 v[34:35], v[34:35], 0, s[36:37]
	v_lshl_add_u64 v[36:37], v[36:37], 0, s[36:37]
	v_lshl_add_u64 v[38:39], v[38:39], 0, s[36:37]
	v_lshl_add_u64 v[40:41], v[40:41], 0, s[36:37]
	v_lshl_add_u64 v[42:43], v[42:43], 0, s[36:37]
	s_cmpk_eq_i32 s38, 0x700
	v_lshl_add_u64 v[44:45], v[44:45], 0, s[40:41]
	ds_write_b128 v18, v[46:49]
	ds_write_b128 v18, v[50:53] offset:272
	s_waitcnt lgkmcnt(0)
	s_barrier
	s_cbranch_scc1 .LBB0_405

.LBB0_598:
	v_cndmask_b32_e64 v2, v2, 0, s[80:81]
	v_cndmask_b32_e64 v1, v1, 0, s[80:81]
	v_cndmask_b32_e64 v12, v12, 0, s[80:81]
	ds_read_b128 v[96:99], v142
	ds_read_b128 v[70:73], v142 offset:16
	v_lshlrev_b32_e32 v100, 16, v2
	v_and_b32_e32 v128, 0xffff0000, v2
	v_lshlrev_b32_e32 v101, 16, v1
	v_and_b32_e32 v129, 0xffff0000, v1
	v_lshlrev_b32_e32 v102, 16, v12
	v_and_b32_e32 v130, 0xffff0000, v12
	v_lshlrev_b32_e32 v103, 16, v3
	v_and_b32_e32 v131, 0xffff0000, v3
	v_lshlrev_b32_e32 v104, 16, v4
	v_and_b32_e32 v132, 0xffff0000, v4
	v_lshlrev_b32_e32 v105, 16, v5
	v_and_b32_e32 v133, 0xffff0000, v5
	v_lshlrev_b32_e32 v106, 16, v6
	v_and_b32_e32 v134, 0xffff0000, v6
	v_lshlrev_b32_e32 v107, 16, v7
	v_and_b32_e32 v135, 0xffff0000, v7
	v_lshlrev_b32_e32 v108, 16, v8
	v_and_b32_e32 v136, 0xffff0000, v8
	v_lshlrev_b32_e32 v109, 16, v9
	v_and_b32_e32 v137, 0xffff0000, v9
	v_lshlrev_b32_e32 v95, 16, v10
	v_and_b32_e32 v138, 0xffff0000, v10
	v_fma_f32 v148, v176, v100, v184
	v_fma_f32 v149, v177, v128, v185
	v_fmac_f32_e32 v148, v178, v101
	v_fmac_f32_e32 v149, v179, v129
	v_fmac_f32_e32 v148, v180, v102
	v_fmac_f32_e32 v149, v181, v130
	v_fmac_f32_e32 v148, v182, v103
	v_fmac_f32_e32 v149, v183, v131
	v_mul_f32_e32 v150, 0xbfb8aa3b, v148
	v_mul_f32_e32 v151, 0xbfb8aa3b, v149
	v_exp_f32_e32 v150, v150
	v_exp_f32_e32 v151, v151
	v_add_f32_e32 v150, 1.0, v150
	v_add_f32_e32 v151, 1.0, v151
	v_rcp_f32_e32 v150, v150
	v_rcp_f32_e32 v151, v151
	s_waitcnt lgkmcnt(0)
	v_mul_f32_e32 v148, v148, v150
	v_mul_f32_e32 v149, v149, v151
	v_mul_f32_e32 v100, v148, v96
	v_mul_f32_e32 v128, v149, v96
	v_fma_f32 v148, v176, v101, v184
	v_fma_f32 v149, v177, v129, v185
	v_fmac_f32_e32 v148, v178, v102
	v_fmac_f32_e32 v149, v179, v130
	v_fmac_f32_e32 v148, v180, v103
	v_fmac_f32_e32 v149, v181, v131
	v_fmac_f32_e32 v148, v182, v104
	v_fmac_f32_e32 v149, v183, v132
	v_mul_f32_e32 v150, 0xbfb8aa3b, v148
	v_mul_f32_e32 v151, 0xbfb8aa3b, v149
	v_exp_f32_e32 v150, v150
	v_exp_f32_e32 v151, v151
	v_add_f32_e32 v150, 1.0, v150
	v_add_f32_e32 v151, 1.0, v151
	v_rcp_f32_e32 v150, v150
	v_rcp_f32_e32 v151, v151
	v_mul_f32_e32 v148, v148, v150
	v_mul_f32_e32 v149, v149, v151
	v_mul_f32_e32 v101, v148, v97
	v_mul_f32_e32 v129, v149, v97
	v_fma_f32 v148, v176, v102, v184
	v_fma_f32 v149, v177, v130, v185
	v_fmac_f32_e32 v148, v178, v103
	v_fmac_f32_e32 v149, v179, v131
	v_fmac_f32_e32 v148, v180, v104
	v_fmac_f32_e32 v149, v181, v132
	v_fmac_f32_e32 v148, v182, v105
	v_fmac_f32_e32 v149, v183, v133
	v_mul_f32_e32 v150, 0xbfb8aa3b, v148
	v_mul_f32_e32 v151, 0xbfb8aa3b, v149
	v_exp_f32_e32 v150, v150
	v_exp_f32_e32 v151, v151
	v_add_f32_e32 v150, 1.0, v150
	v_add_f32_e32 v151, 1.0, v151
	v_rcp_f32_e32 v150, v150
	v_rcp_f32_e32 v151, v151
	v_mul_f32_e32 v148, v148, v150
	v_mul_f32_e32 v149, v149, v151
	v_mul_f32_e32 v102, v148, v98
	v_mul_f32_e32 v130, v149, v98
	v_fma_f32 v148, v176, v103, v184
	v_fma_f32 v149, v177, v131, v185
	v_fmac_f32_e32 v148, v178, v104
	v_fmac_f32_e32 v149, v179, v132
	v_fmac_f32_e32 v148, v180, v105
	v_fmac_f32_e32 v149, v181, v133
	v_fmac_f32_e32 v148, v182, v106
	v_fmac_f32_e32 v149, v183, v134
	v_mul_f32_e32 v150, 0xbfb8aa3b, v148
	v_mul_f32_e32 v151, 0xbfb8aa3b, v149
	v_exp_f32_e32 v150, v150
	v_exp_f32_e32 v151, v151
	v_add_f32_e32 v150, 1.0, v150
	v_add_f32_e32 v151, 1.0, v151
	v_rcp_f32_e32 v150, v150
	v_rcp_f32_e32 v151, v151
	v_mul_f32_e32 v148, v148, v150
	v_mul_f32_e32 v149, v149, v151
	v_mul_f32_e32 v103, v148, v99
	v_mul_f32_e32 v131, v149, v99
	v_fma_f32 v148, v176, v104, v184
	v_fma_f32 v149, v177, v132, v185
	v_fmac_f32_e32 v148, v178, v105
	v_fmac_f32_e32 v149, v179, v133
	v_fmac_f32_e32 v148, v180, v106
	v_fmac_f32_e32 v149, v181, v134
	v_fmac_f32_e32 v148, v182, v107
	v_fmac_f32_e32 v149, v183, v135
	v_mul_f32_e32 v150, 0xbfb8aa3b, v148
	v_mul_f32_e32 v151, 0xbfb8aa3b, v149
	v_exp_f32_e32 v150, v150
	v_exp_f32_e32 v151, v151
	v_add_f32_e32 v150, 1.0, v150
	v_add_f32_e32 v151, 1.0, v151
	v_rcp_f32_e32 v150, v150
	v_rcp_f32_e32 v151, v151
	v_mul_f32_e32 v148, v148, v150
	v_mul_f32_e32 v149, v149, v151
	v_mul_f32_e32 v104, v148, v70
	v_mul_f32_e32 v132, v149, v70
	v_fma_f32 v148, v176, v105, v184
	v_fma_f32 v149, v177, v133, v185
	v_fmac_f32_e32 v148, v178, v106
	v_fmac_f32_e32 v149, v179, v134
	v_fmac_f32_e32 v148, v180, v107
	v_fmac_f32_e32 v149, v181, v135
	v_fmac_f32_e32 v148, v182, v108
	v_fmac_f32_e32 v149, v183, v136
	v_mul_f32_e32 v150, 0xbfb8aa3b, v148
	v_mul_f32_e32 v151, 0xbfb8aa3b, v149
	v_exp_f32_e32 v150, v150
	v_exp_f32_e32 v151, v151
	v_add_f32_e32 v150, 1.0, v150
	v_add_f32_e32 v151, 1.0, v151
	v_rcp_f32_e32 v150, v150
	v_rcp_f32_e32 v151, v151
	v_mul_f32_e32 v148, v148, v150
	v_mul_f32_e32 v149, v149, v151
	v_mul_f32_e32 v105, v148, v71
	v_mul_f32_e32 v133, v149, v71
	v_fma_f32 v148, v176, v106, v184
	v_fma_f32 v149, v177, v134, v185
	v_fmac_f32_e32 v148, v178, v107
	v_fmac_f32_e32 v149, v179, v135
	v_fmac_f32_e32 v148, v180, v108
	v_fmac_f32_e32 v149, v181, v136
	v_fmac_f32_e32 v148, v182, v109
	v_fmac_f32_e32 v149, v183, v137
	v_mul_f32_e32 v150, 0xbfb8aa3b, v148
	v_mul_f32_e32 v151, 0xbfb8aa3b, v149
	v_exp_f32_e32 v150, v150
	v_exp_f32_e32 v151, v151
	v_add_f32_e32 v150, 1.0, v150
	v_add_f32_e32 v151, 1.0, v151
	v_rcp_f32_e32 v150, v150
	v_rcp_f32_e32 v151, v151
	v_mul_f32_e32 v148, v148, v150
	v_mul_f32_e32 v149, v149, v151
	v_mul_f32_e32 v106, v148, v72
	v_mul_f32_e32 v134, v149, v72
	v_fma_f32 v148, v176, v107, v184
	v_fma_f32 v149, v177, v135, v185
	v_fmac_f32_e32 v148, v178, v108
	v_fmac_f32_e32 v149, v179, v136
	v_fmac_f32_e32 v148, v180, v109
	v_fmac_f32_e32 v149, v181, v137
	v_fmac_f32_e32 v148, v182, v95
	v_fmac_f32_e32 v149, v183, v138
	v_mul_f32_e32 v150, 0xbfb8aa3b, v148
	v_mul_f32_e32 v151, 0xbfb8aa3b, v149
	v_exp_f32_e32 v150, v150
	v_exp_f32_e32 v151, v151
	v_add_f32_e32 v150, 1.0, v150
	v_add_f32_e32 v151, 1.0, v151
	v_rcp_f32_e32 v150, v150
	v_rcp_f32_e32 v151, v151
	v_mul_f32_e32 v148, v148, v150
	v_mul_f32_e32 v149, v149, v151
	v_mul_f32_e32 v107, v148, v73
	v_mul_f32_e32 v135, v149, v73
	s_and_b64 s[4:5], s[90:91], exec
	s_cselect_b32 s4, s51, s33
	s_add_i32 s6, 0, 0xec00
	v_cvt_pk_bf16_f32 v70, v100, v101
	v_cvt_pk_bf16_f32 v71, v102, v103
	v_cvt_pk_bf16_f32 v72, v104, v105
	v_cvt_pk_bf16_f32 v73, v106, v107
	v_cvt_pk_bf16_f32 v74, v128, v129
	v_cvt_pk_bf16_f32 v75, v130, v131
	v_cvt_pk_bf16_f32 v76, v132, v133
	v_cvt_pk_bf16_f32 v77, v134, v135
	v_add3_u32 v81, s4, v225, v226
	s_and_b64 s[4:5], s[90:91], exec
	s_cselect_b32 s4, s6, s10
	ds_write_b128 v81, v[70:73]
	ds_write_b128 v81, v[74:77] offset:272
	v_add3_u32 v70, s4, v228, v158
	ds_write_b128 v70, v[14:17]
	v_add3_u32 v70, s4, v230, v158
	ds_write_b128 v70, v[18:21]
	s_branch .LBB0_564

.LBB0_932:
	s_add_u32 s16, s92, 0x7a100000
	s_addc_u32 s17, s93, 0
	s_lshl_b32 s0, s18, 5
	s_and_b32 s5, s0, 0x60
	s_lshl_b32 s4, s9, 13
	s_lshl_b32 s6, s5, 7
	s_add_i32 s53, s37, 0x18000
	s_mov_b64 s[18:19], 0x80
	s_add_i32 s54, s37, 0x1a000
	v_lshl_add_u64 v[4:5], v[4:5], 0, s[18:19]
	s_mov_b32 m0, s53
	s_add_u32 s20, s92, 0x35c00080
	s_waitcnt vmcnt(2)
	s_barrier
	global_load_lds_dwordx4 v[4:5], off
	v_lshl_add_u64 v[2:3], v[2:3], 0, s[18:19]
	s_mov_b32 m0, s54
	s_addc_u32 s21, s93, 0
	s_add_i32 s55, s37, 0x8000
	s_add_i32 s56, s37, 0xa000
	global_load_lds_dwordx4 v[2:3], off
	v_lshl_add_u64 v[2:3], s[20:21], 0, v[66:67]
	s_mov_b32 m0, s55
	s_add_u32 s0, s40, 0x40080
	global_load_lds_dwordx4 v[2:3], off
	v_lshl_add_u64 v[2:3], s[20:21], 0, v[206:207]
	s_mov_b32 m0, s56
	s_addc_u32 s1, s41, 0
	s_add_i32 s57, s37, 0x1c000
	global_load_lds_dwordx4 v[2:3], off
	v_lshl_add_u64 v[2:3], s[0:1], 0, v[202:203]
	s_mov_b32 m0, s57
	s_add_i32 s58, s37, 0x1e000
	global_load_lds_dwordx4 v[2:3], off
	v_lshl_add_u64 v[2:3], s[0:1], 0, v[204:205]
	s_mov_b32 m0, s58
	v_lshlrev_b32_e32 v4, 6, v0
	global_load_lds_dwordx4 v[2:3], off
	v_and_b32_e32 v2, 15, v0
	v_lshlrev_b32_e32 v3, 1, v6
	s_movk_i32 s0, 0x3c0
	v_lshl_or_b32 v220, s9, 6, v2
	v_lshl_or_b32 v2, v2, 6, v3
	v_and_or_b32 v3, v4, s0, v3
	v_lshlrev_b32_e32 v4, 2, v0
	v_and_b32_e32 v4, 32, v4
	s_waitcnt vmcnt(6)
	s_add_i32 s0, s6, 0
	v_xad_u32 v3, v3, v4, s0
	v_xad_u32 v2, v2, v4, 0
	s_cmpk_lt_u32 s8, 0x100
	s_cselect_b64 s[22:23], -1, 0
	v_add_u32_e32 v221, 0x10000, v3
	v_add_u32_e32 v222, 0x10400, v3
	v_add_u32_e32 v223, 0x10800, v3
	v_add_u32_e32 v224, 0x10c00, v3
	v_add_u32_e32 v225, 0x14000, v3
	v_add_u32_e32 v226, 0x14400, v3
	v_add_u32_e32 v227, 0x14800, v3
	v_add_u32_e32 v228, 0x14c00, v3
	v_add_u32_e32 v229, 0x18000, v3
	v_add_u32_e32 v230, 0x18400, v3
	v_add_u32_e32 v231, 0x18800, v3
	v_add_u32_e32 v232, 0x18c00, v3
	v_add_u32_e32 v233, 0x1c000, v3
	v_add_u32_e32 v234, 0x1c400, v3
	v_add_u32_e32 v235, 0x1c800, v3
	v_add_u32_e32 v236, 0x1cc00, v3
	s_ashr_i32 s59, s83, 31
	v_ashrrev_i32_e32 v201, 31, v200
	v_or_b32_e32 v237, s5, v6
	v_add_u32_e32 v238, s4, v2
	s_mov_b64 s[24:25], 0x2000
	s_mov_b32 s26, 0x3d000000
	s_mov_b32 s60, 0xc0c00000
	s_mov_b32 s61, 0x40000
	s_mov_b32 s62, 0x48000
	s_mov_b32 s63, 0x50000
	v_mov_b32_e32 v239, 0x41000000
	s_barrier
	s_branch .LBB0_935

.LBB0_950:
	s_nop 15
	s_nop 15
	v_lshl_add_u32 v22, s65, 8, v220
	v_readlane_b32 s69, v253, 5
	v_readlane_b32 s72, v253, 8
	v_readlane_b32 s73, v253, 9
	v_readlane_b32 s74, v253, 10
	v_readlane_b32 s75, v253, 11
	s_waitcnt vmcnt(0)
	v_add_f32_e32 v14, 1.0, v14
	v_add_f32_e32 v15, 1.0, v15
	v_add_f32_e32 v16, 1.0, v16
	v_add_f32_e32 v17, 1.0, v17
	v_add_f32_e32 v2, 1.0, v2
	v_add_f32_e32 v3, 1.0, v3
	v_add_f32_e32 v4, 1.0, v4
	v_add_f32_e32 v5, 1.0, v5
	v_pk_fma_f32 v[26:27], v[196:197], s[26:27], v[10:11] op_sel_hi:[1,0,1]
	s_nop 0
	v_min_f32_e32 v23, 0x40e00000, v26
	v_min_f32_e32 v25, 0x40e00000, v27
	v_mul_f32_e32 v38, 0xc01d265f, v23
	v_mul_f32_e32 v39, 0xc01d265f, v25
	v_pk_fma_f32 v[18:19], v[198:199], s[26:27], v[12:13] op_sel_hi:[1,0,1]
	v_exp_f32_e32 v38, v38
	v_exp_f32_e32 v39, v39
	v_min_f32_e32 v32, 0x40e00000, v18
	v_min_f32_e32 v33, 0x40e00000, v19
	v_pk_fma_f32 v[30:31], v[192:193], s[26:27], v[6:7] op_sel_hi:[1,0,1]
	v_mul_f32_e32 v40, 0xc01d265f, v32
	v_mul_f32_e32 v41, 0xc01d265f, v33
	v_min_f32_e32 v34, 0x40e00000, v30
	v_min_f32_e32 v35, 0x40e00000, v31
	v_mul_f32_e32 v42, 0xc01d265f, v34
	v_mul_f32_e32 v43, 0xc01d265f, v35
	v_exp_f32_e32 v40, v40
	v_exp_f32_e32 v41, v41
	v_add_f32_e32 v38, 1.0, v38
	v_add_f32_e32 v39, 1.0, v39
	v_rcp_f32_e32 v38, v38
	v_rcp_f32_e32 v39, v39
	v_pk_fma_f32 v[28:29], v[194:195], s[26:27], v[8:9] op_sel_hi:[1,0,1]
	v_exp_f32_e32 v42, v42
	v_exp_f32_e32 v43, v43
	v_min_f32_e32 v36, 0x40e00000, v28
	v_min_f32_e32 v37, 0x40e00000, v29
	v_pk_fma_f32 v[26:27], v[188:189], s[26:27], v[14:15] op_sel_hi:[1,0,1]
	v_mul_f32_e32 v44, 0xc01d265f, v36
	v_mul_f32_e32 v45, 0xc01d265f, v37
	v_med3_f32 v26, v26, s60, v239
	v_med3_f32 v27, v27, s60, v239
	v_add_f32_e32 v40, 1.0, v40
	v_add_f32_e32 v41, 1.0, v41
	v_rcp_f32_e32 v40, v40
	v_rcp_f32_e32 v41, v41
	v_mul_f32_e32 v23, v23, v38
	v_mul_f32_e32 v25, v25, v39
	v_exp_f32_e32 v44, v44
	v_exp_f32_e32 v45, v45
	v_add_f32_e32 v42, 1.0, v42
	v_add_f32_e32 v43, 1.0, v43
	v_mul_f32_e32 v23, v26, v23
	v_mul_f32_e32 v25, v27, v25
	v_pk_fma_f32 v[18:19], v[190:191], s[26:27], v[16:17] op_sel_hi:[1,0,1]
	v_rcp_f32_e32 v42, v42
	v_rcp_f32_e32 v43, v43
	v_cvt_pk_fp8_f32 v24, v23, v25
	v_med3_f32 v18, v18, s60, v239
	v_med3_f32 v19, v19, s60, v239
	v_pk_fma_f32 v[30:31], v[184:185], s[26:27], v[2:3] op_sel_hi:[1,0,1]
	v_mul_f32_e32 v32, v32, v40
	v_mul_f32_e32 v33, v33, v41
	v_med3_f32 v30, v30, s60, v239
	v_med3_f32 v31, v31, s60, v239
	v_add_f32_e32 v44, 1.0, v44
	v_add_f32_e32 v45, 1.0, v45
	v_mul_f32_e32 v18, v18, v32
	v_mul_f32_e32 v19, v19, v33
	v_rcp_f32_e32 v44, v44
	v_mul_f32_e32 v34, v34, v42
	v_mul_f32_e32 v35, v35, v43
	v_cvt_pk_fp8_f32 v24, v18, v19 op_sel:[0,0,1]
	v_rcp_f32_e32 v18, v45
	v_mul_f32_e32 v23, v30, v34
	v_mul_f32_e32 v26, v31, v35
	v_mov_b32_e32 v25, v67
	v_pk_fma_f32 v[28:29], v[186:187], s[26:27], v[4:5] op_sel_hi:[1,0,1]
	v_cvt_pk_fp8_f32 v25, v23, v26
	v_med3_f32 v28, v28, s60, v239
	v_med3_f32 v19, v29, s60, v239
	v_mul_f32_e32 v36, v36, v44
	v_mul_f32_e32 v18, v37, v18
	v_mul_f32_e32 v27, v28, v36
	v_mul_f32_e32 v18, v19, v18
	v_cvt_pk_fp8_f32 v25, v27, v18 op_sel:[0,0,1]
	v_ashrrev_i32_e32 v23, 31, v22
	v_pk_fma_f32 v[26:27], v[180:181], s[26:27], v[10:11] op_sel_hi:[1,0,1]
	v_lshlrev_b64 v[18:19], 11, v[22:23]
	v_min_f32_e32 v23, 0x40e00000, v26
	v_mul_f32_e32 v26, 0xc01d265f, v23
	v_exp_f32_e32 v26, v26
	v_min_f32_e32 v27, 0x40e00000, v27
	v_mul_f32_e32 v40, 0xc01d265f, v27
	v_add_f32_e32 v26, 1.0, v26
	v_rcp_f32_e32 v26, v26
	v_exp_f32_e32 v40, v40
	v_pk_fma_f32 v[34:35], v[172:173], s[26:27], v[14:15] op_sel_hi:[1,0,1]
	v_lshl_add_u64 v[18:19], s[16:17], 0, v[18:19]
	v_med3_f32 v34, v34, s60, v239
	v_mul_f32_e32 v23, v23, v26
	v_mov_b32_e32 v26, v34
	v_lshl_add_u64 v[18:19], v[18:19], 0, v[20:21]
	v_mul_f32_e32 v23, v26, v23
	v_add_f32_e32 v26, 1.0, v40
	global_store_dwordx2 v[18:19], v[24:25], off
	v_pk_fma_f32 v[24:25], v[182:183], s[26:27], v[12:13] op_sel_hi:[1,0,1]
	v_rcp_f32_e32 v26, v26
	v_min_f32_e32 v24, 0x40e00000, v24
	v_mul_f32_e32 v34, 0xc01d265f, v24
	v_med3_f32 v35, v35, s60, v239
	v_min_f32_e32 v25, 0x40e00000, v25
	v_exp_f32_e32 v34, v34
	v_mul_f32_e32 v26, v27, v26
	v_mov_b32_e32 v27, v35
	v_mul_f32_e32 v35, 0xc01d265f, v25
	v_exp_f32_e32 v35, v35
	v_add_f32_e32 v34, 1.0, v34
	v_pk_fma_f32 v[32:33], v[174:175], s[26:27], v[16:17] op_sel_hi:[1,0,1]
	v_rcp_f32_e32 v34, v34
	v_mul_f32_e32 v26, v27, v26
	v_med3_f32 v27, v32, s60, v239
	v_add_f32_e32 v32, 1.0, v35
	v_rcp_f32_e32 v32, v32
	v_mul_f32_e32 v24, v24, v34
	v_mul_f32_e32 v27, v27, v24
	v_med3_f32 v24, v33, s60, v239
	v_mul_f32_e32 v25, v25, v32
	v_pk_fma_f32 v[30:31], v[176:177], s[26:27], v[6:7] op_sel_hi:[1,0,1]
	v_mul_f32_e32 v25, v24, v25
	v_mov_b32_e32 v24, v67
	v_cvt_pk_fp8_f32 v24, v23, v26
	v_min_f32_e32 v26, 0x40e00000, v31
	v_mul_f32_e32 v31, 0xc01d265f, v26
	v_exp_f32_e32 v31, v31
	v_min_f32_e32 v30, 0x40e00000, v30
	v_cvt_pk_fp8_f32 v24, v27, v25 op_sel:[0,0,1]
	v_mul_f32_e32 v32, 0xc01d265f, v30
	v_add_f32_e32 v27, 1.0, v31
	v_rcp_f32_e32 v27, v27
	v_exp_f32_e32 v32, v32
	v_pk_fma_f32 v[28:29], v[178:179], s[26:27], v[8:9] op_sel_hi:[1,0,1]
	v_mul_f32_e32 v26, v26, v27
	v_min_f32_e32 v27, 0x40e00000, v28
	v_mul_f32_e32 v28, 0xc01d265f, v27
	v_add_f32_e32 v23, 1.0, v32
	v_rcp_f32_e32 v23, v23
	v_exp_f32_e32 v28, v28
	v_pk_fma_f32 v[38:39], v[168:169], s[26:27], v[2:3] op_sel_hi:[1,0,1]
	v_min_f32_e32 v29, 0x40e00000, v29
	v_med3_f32 v25, v38, s60, v239
	v_mul_f32_e32 v23, v30, v23
	v_add_f32_e32 v28, 1.0, v28
	v_mul_f32_e32 v30, 0xc01d265f, v29
	v_rcp_f32_e32 v28, v28
	v_mul_f32_e32 v23, v25, v23
	v_med3_f32 v25, v39, s60, v239
	v_exp_f32_e32 v30, v30
	v_pk_fma_f32 v[36:37], v[170:171], s[26:27], v[4:5] op_sel_hi:[1,0,1]
	v_mul_f32_e32 v26, v25, v26
	v_med3_f32 v25, v36, s60, v239
	v_mul_f32_e32 v27, v27, v28
	v_mul_f32_e32 v27, v25, v27
	v_add_f32_e32 v25, 1.0, v30
	v_rcp_f32_e32 v28, v25
	v_mov_b32_e32 v25, v67
	v_cvt_pk_fp8_f32 v25, v23, v26
	v_med3_f32 v30, v37, s60, v239
	v_mul_f32_e32 v23, v29, v28
	v_mov_b32_e32 v26, v30
	v_mul_f32_e32 v23, v26, v23
	v_or_b32_e32 v26, 16, v22
	v_cvt_pk_fp8_f32 v25, v27, v23 op_sel:[0,0,1]
	v_ashrrev_i32_e32 v27, 31, v26
	v_lshlrev_b64 v[26:27], 11, v[26:27]
	v_lshl_add_u64 v[26:27], s[16:17], 0, v[26:27]
	v_lshl_add_u64 v[26:27], v[26:27], 0, v[20:21]
	global_store_dwordx2 v[26:27], v[24:25], off
	v_pk_fma_f32 v[26:27], v[164:165], s[26:27], v[10:11] op_sel_hi:[1,0,1]
	v_pk_fma_f32 v[34:35], v[156:157], s[26:27], v[14:15] op_sel_hi:[1,0,1]
	v_min_f32_e32 v23, 0x40e00000, v26
	v_mul_f32_e32 v26, 0xc01d265f, v23
	v_exp_f32_e32 v26, v26
	v_min_f32_e32 v27, 0x40e00000, v27
	v_mul_f32_e32 v40, 0xc01d265f, v27
	v_add_f32_e32 v26, 1.0, v26
	v_rcp_f32_e32 v26, v26
	v_exp_f32_e32 v40, v40
	v_med3_f32 v34, v34, s60, v239
	v_pk_fma_f32 v[24:25], v[166:167], s[26:27], v[12:13] op_sel_hi:[1,0,1]
	v_mul_f32_e32 v23, v23, v26
	v_mov_b32_e32 v26, v34
	v_mul_f32_e32 v23, v26, v23
	v_add_f32_e32 v26, 1.0, v40
	v_rcp_f32_e32 v26, v26
	v_min_f32_e32 v24, 0x40e00000, v24
	v_mul_f32_e32 v34, 0xc01d265f, v24
	v_med3_f32 v35, v35, s60, v239
	v_min_f32_e32 v25, 0x40e00000, v25
	v_exp_f32_e32 v34, v34
	v_mul_f32_e32 v26, v27, v26
	v_mov_b32_e32 v27, v35
	v_mul_f32_e32 v35, 0xc01d265f, v25
	v_exp_f32_e32 v35, v35
	v_add_f32_e32 v34, 1.0, v34
	v_pk_fma_f32 v[32:33], v[158:159], s[26:27], v[16:17] op_sel_hi:[1,0,1]
	v_rcp_f32_e32 v34, v34
	v_mul_f32_e32 v26, v27, v26
	v_med3_f32 v27, v32, s60, v239
	v_add_f32_e32 v32, 1.0, v35
	v_rcp_f32_e32 v32, v32
	v_mul_f32_e32 v24, v24, v34
	v_mul_f32_e32 v27, v27, v24
	v_med3_f32 v24, v33, s60, v239
	v_mul_f32_e32 v25, v25, v32
	v_pk_fma_f32 v[30:31], v[160:161], s[26:27], v[6:7] op_sel_hi:[1,0,1]
	v_mul_f32_e32 v25, v24, v25
	v_mov_b32_e32 v24, v67
	v_cvt_pk_fp8_f32 v24, v23, v26
	v_min_f32_e32 v26, 0x40e00000, v31
	v_mul_f32_e32 v31, 0xc01d265f, v26
	v_exp_f32_e32 v31, v31
	v_min_f32_e32 v30, 0x40e00000, v30
	v_cvt_pk_fp8_f32 v24, v27, v25 op_sel:[0,0,1]
	v_mul_f32_e32 v32, 0xc01d265f, v30
	v_add_f32_e32 v27, 1.0, v31
	v_rcp_f32_e32 v27, v27
	v_exp_f32_e32 v32, v32
	v_pk_fma_f32 v[28:29], v[162:163], s[26:27], v[8:9] op_sel_hi:[1,0,1]
	v_mul_f32_e32 v26, v26, v27
	v_min_f32_e32 v27, 0x40e00000, v28
	v_mul_f32_e32 v28, 0xc01d265f, v27
	v_add_f32_e32 v23, 1.0, v32
	v_rcp_f32_e32 v23, v23
	v_exp_f32_e32 v28, v28
	v_pk_fma_f32 v[38:39], v[152:153], s[26:27], v[2:3] op_sel_hi:[1,0,1]
	v_min_f32_e32 v29, 0x40e00000, v29
	v_med3_f32 v25, v38, s60, v239
	v_mul_f32_e32 v23, v30, v23
	v_add_f32_e32 v28, 1.0, v28
	v_mul_f32_e32 v30, 0xc01d265f, v29
	v_rcp_f32_e32 v28, v28
	v_mul_f32_e32 v23, v25, v23
	v_med3_f32 v25, v39, s60, v239
	v_exp_f32_e32 v30, v30
	v_pk_fma_f32 v[36:37], v[154:155], s[26:27], v[4:5] op_sel_hi:[1,0,1]
	v_mul_f32_e32 v26, v25, v26
	v_med3_f32 v25, v36, s60, v239
	v_mul_f32_e32 v27, v27, v28
	v_mul_f32_e32 v27, v25, v27
	v_add_f32_e32 v25, 1.0, v30
	v_rcp_f32_e32 v28, v25
	v_mov_b32_e32 v25, v67
	v_cvt_pk_fp8_f32 v25, v23, v26
	v_med3_f32 v30, v37, s60, v239
	v_mul_f32_e32 v23, v29, v28
	v_mov_b32_e32 v26, v30
	v_mul_f32_e32 v23, v26, v23
	v_or_b32_e32 v26, 32, v22
	v_cvt_pk_fp8_f32 v25, v27, v23 op_sel:[0,0,1]
	v_ashrrev_i32_e32 v27, 31, v26
	v_lshlrev_b64 v[26:27], 11, v[26:27]
	v_lshl_add_u64 v[26:27], s[16:17], 0, v[26:27]
	v_lshl_add_u64 v[26:27], v[26:27], 0, v[20:21]
	global_store_dwordx2 v[26:27], v[24:25], off
	v_pk_fma_f32 v[26:27], v[148:149], s[26:27], v[10:11] op_sel_hi:[1,0,1]
	v_pk_fma_f32 v[34:35], v[140:141], s[26:27], v[14:15] op_sel_hi:[1,0,1]
	v_min_f32_e32 v23, 0x40e00000, v26
	v_mul_f32_e32 v26, 0xc01d265f, v23
	v_exp_f32_e32 v26, v26
	v_min_f32_e32 v27, 0x40e00000, v27
	v_mul_f32_e32 v40, 0xc01d265f, v27
	v_add_f32_e32 v26, 1.0, v26
	v_rcp_f32_e32 v26, v26
	v_exp_f32_e32 v40, v40
	v_med3_f32 v34, v34, s60, v239
	v_pk_fma_f32 v[24:25], v[150:151], s[26:27], v[12:13] op_sel_hi:[1,0,1]
	v_mul_f32_e32 v23, v23, v26
	v_mov_b32_e32 v26, v34
	v_mul_f32_e32 v23, v26, v23
	v_add_f32_e32 v26, 1.0, v40
	v_rcp_f32_e32 v26, v26
	v_min_f32_e32 v24, 0x40e00000, v24
	v_mul_f32_e32 v34, 0xc01d265f, v24
	v_med3_f32 v35, v35, s60, v239
	v_min_f32_e32 v25, 0x40e00000, v25
	v_exp_f32_e32 v34, v34
	v_mul_f32_e32 v26, v27, v26
	v_mov_b32_e32 v27, v35
	v_mul_f32_e32 v35, 0xc01d265f, v25
	v_exp_f32_e32 v35, v35
	v_add_f32_e32 v34, 1.0, v34
	v_pk_fma_f32 v[32:33], v[142:143], s[26:27], v[16:17] op_sel_hi:[1,0,1]
	v_rcp_f32_e32 v34, v34
	v_mul_f32_e32 v26, v27, v26
	v_med3_f32 v27, v32, s60, v239
	v_add_f32_e32 v32, 1.0, v35
	v_rcp_f32_e32 v32, v32
	v_mul_f32_e32 v24, v24, v34
	v_mul_f32_e32 v27, v27, v24
	v_med3_f32 v24, v33, s60, v239
	v_mul_f32_e32 v25, v25, v32
	v_pk_fma_f32 v[30:31], v[144:145], s[26:27], v[6:7] op_sel_hi:[1,0,1]
	v_mul_f32_e32 v25, v24, v25
	v_mov_b32_e32 v24, v67
	v_cvt_pk_fp8_f32 v24, v23, v26
	v_min_f32_e32 v26, 0x40e00000, v31
	v_mul_f32_e32 v31, 0xc01d265f, v26
	v_exp_f32_e32 v31, v31
	v_min_f32_e32 v30, 0x40e00000, v30
	v_cvt_pk_fp8_f32 v24, v27, v25 op_sel:[0,0,1]
	v_mul_f32_e32 v32, 0xc01d265f, v30
	v_add_f32_e32 v27, 1.0, v31
	v_rcp_f32_e32 v27, v27
	v_exp_f32_e32 v32, v32
	v_pk_fma_f32 v[28:29], v[146:147], s[26:27], v[8:9] op_sel_hi:[1,0,1]
	v_mul_f32_e32 v26, v26, v27
	v_min_f32_e32 v27, 0x40e00000, v28
	v_mul_f32_e32 v28, 0xc01d265f, v27
	v_add_f32_e32 v23, 1.0, v32
	v_rcp_f32_e32 v23, v23
	v_exp_f32_e32 v28, v28
	v_pk_fma_f32 v[38:39], v[136:137], s[26:27], v[2:3] op_sel_hi:[1,0,1]
	v_min_f32_e32 v29, 0x40e00000, v29
	v_med3_f32 v25, v38, s60, v239
	v_mul_f32_e32 v23, v30, v23
	v_add_f32_e32 v28, 1.0, v28
	v_mul_f32_e32 v30, 0xc01d265f, v29
	v_rcp_f32_e32 v28, v28
	v_mul_f32_e32 v23, v25, v23
	v_med3_f32 v25, v39, s60, v239
	v_exp_f32_e32 v30, v30
	v_pk_fma_f32 v[36:37], v[138:139], s[26:27], v[4:5] op_sel_hi:[1,0,1]
	v_mul_f32_e32 v26, v25, v26
	v_med3_f32 v25, v36, s60, v239
	v_mul_f32_e32 v27, v27, v28
	v_mul_f32_e32 v27, v25, v27
	v_add_f32_e32 v25, 1.0, v30
	v_rcp_f32_e32 v28, v25
	v_mov_b32_e32 v25, v67
	v_cvt_pk_fp8_f32 v25, v23, v26
	v_med3_f32 v30, v37, s60, v239
	v_mul_f32_e32 v23, v29, v28
	v_mov_b32_e32 v26, v30
	v_mul_f32_e32 v23, v26, v23
	v_or_b32_e32 v22, 48, v22
	v_cvt_pk_fp8_f32 v25, v27, v23 op_sel:[0,0,1]
	v_ashrrev_i32_e32 v23, 31, v22
	v_lshlrev_b64 v[22:23], 11, v[22:23]
	v_lshl_add_u64 v[22:23], s[16:17], 0, v[22:23]
	v_lshl_add_u64 v[20:21], v[22:23], 0, v[20:21]
	v_pk_fma_f32 v[22:23], v[132:133], s[26:27], v[10:11] op_sel_hi:[1,0,1]
	global_store_dwordx2 v[20:21], v[24:25], off
	v_min_f32_e32 v22, 0x40e00000, v22
	v_mul_f32_e32 v32, 0xc01d265f, v22
	v_exp_f32_e32 v36, v32
	v_min_f32_e32 v23, 0x40e00000, v23
	v_mul_f32_e32 v37, 0xc01d265f, v23
	v_add_f32_e32 v36, 1.0, v36
	v_rcp_f32_e32 v36, v36
	v_exp_f32_e32 v37, v37
	v_pk_fma_f32 v[20:21], v[134:135], s[26:27], v[12:13] op_sel_hi:[1,0,1]
	v_pk_fma_f32 v[30:31], v[124:125], s[26:27], v[14:15] op_sel_hi:[1,0,1]
	v_min_f32_e32 v20, 0x40e00000, v20
	v_med3_f32 v30, v30, s60, v239
	v_mul_f32_e32 v22, v22, v36
	v_mul_f32_e32 v36, 0xc01d265f, v20
	v_mul_f32_e32 v22, v30, v22
	v_add_f32_e32 v30, 1.0, v37
	v_rcp_f32_e32 v30, v30
	v_exp_f32_e32 v36, v36
	v_med3_f32 v31, v31, s60, v239
	v_min_f32_e32 v21, 0x40e00000, v21
	v_mul_f32_e32 v23, v23, v30
	v_mov_b32_e32 v30, v31
	v_add_f32_e32 v31, 1.0, v36
	v_mul_f32_e32 v36, 0xc01d265f, v21
	v_exp_f32_e32 v36, v36
	v_rcp_f32_e32 v31, v31
	v_pk_fma_f32 v[28:29], v[126:127], s[26:27], v[16:17] op_sel_hi:[1,0,1]
	v_mul_f32_e32 v23, v30, v23
	v_add_f32_e32 v30, 1.0, v36
	v_pk_fma_f32 v[26:27], v[128:129], s[26:27], v[6:7] op_sel_hi:[1,0,1]
	v_med3_f32 v28, v28, s60, v239
	v_rcp_f32_e32 v30, v30
	v_mul_f32_e32 v20, v20, v31
	v_min_f32_e32 v26, 0x40e00000, v26
	v_mul_f32_e32 v28, v28, v20
	v_med3_f32 v20, v29, s60, v239
	v_mul_f32_e32 v29, 0xc01d265f, v26
	v_mul_f32_e32 v21, v21, v30
	v_exp_f32_e32 v29, v29
	v_mul_f32_e32 v21, v20, v21
	v_mov_b32_e32 v20, v67
	v_cvt_pk_fp8_f32 v20, v22, v23
	v_min_f32_e32 v23, 0x40e00000, v27
	v_mul_f32_e32 v27, 0xc01d265f, v23
	v_add_f32_e32 v22, 1.0, v29
	v_rcp_f32_e32 v22, v22
	v_exp_f32_e32 v27, v27
	v_pk_fma_f32 v[24:25], v[130:131], s[26:27], v[8:9] op_sel_hi:[1,0,1]
	v_pk_fma_f32 v[34:35], v[120:121], s[26:27], v[2:3] op_sel_hi:[1,0,1]
	v_mul_f32_e32 v22, v26, v22
	v_add_f32_e32 v26, 1.0, v27
	v_rcp_f32_e32 v26, v26
	v_min_f32_e32 v24, 0x40e00000, v24
	v_min_f32_e32 v25, 0x40e00000, v25
	v_cvt_pk_fp8_f32 v20, v28, v21 op_sel:[0,0,1]
	v_mul_f32_e32 v23, v23, v26
	v_mul_f32_e32 v26, 0xc01d265f, v24
	v_exp_f32_e32 v26, v26
	v_med3_f32 v21, v34, s60, v239
	v_mul_f32_e32 v27, 0xc01d265f, v25
	v_add_f32_e32 v26, 1.0, v26
	v_rcp_f32_e32 v26, v26
	v_mul_f32_e32 v22, v21, v22
	v_med3_f32 v21, v35, s60, v239
	v_exp_f32_e32 v27, v27
	v_pk_fma_f32 v[32:33], v[122:123], s[26:27], v[4:5] op_sel_hi:[1,0,1]
	v_mul_f32_e32 v23, v21, v23
	v_med3_f32 v21, v32, s60, v239
	v_mul_f32_e32 v24, v24, v26
	v_mul_f32_e32 v24, v21, v24
	v_add_f32_e32 v21, 1.0, v27
	v_rcp_f32_e32 v26, v21
	v_mov_b32_e32 v21, v67
	v_cvt_pk_fp8_f32 v21, v22, v23
	v_med3_f32 v27, v33, s60, v239
	v_mul_f32_e32 v22, v25, v26
	v_mov_b32_e32 v23, v27
	v_mul_f32_e32 v22, v23, v22
	v_cvt_pk_fp8_f32 v21, v24, v22 op_sel:[0,0,1]
	v_add_co_u32_e32 v22, vcc, s61, v18
	v_pk_fma_f32 v[30:31], v[108:109], s[26:27], v[14:15] op_sel_hi:[1,0,1]
	s_nop 0
	v_addc_co_u32_e32 v23, vcc, 0, v19, vcc
	global_store_dwordx2 v[22:23], v[20:21], off
	v_pk_fma_f32 v[22:23], v[116:117], s[26:27], v[10:11] op_sel_hi:[1,0,1]
	v_pk_fma_f32 v[20:21], v[118:119], s[26:27], v[12:13] op_sel_hi:[1,0,1]
	v_min_f32_e32 v22, 0x40e00000, v22
	v_mul_f32_e32 v32, 0xc01d265f, v22
	v_exp_f32_e32 v36, v32
	v_min_f32_e32 v23, 0x40e00000, v23
	v_mul_f32_e32 v37, 0xc01d265f, v23
	v_add_f32_e32 v36, 1.0, v36
	v_rcp_f32_e32 v36, v36
	v_exp_f32_e32 v37, v37
	v_med3_f32 v30, v30, s60, v239
	v_min_f32_e32 v20, 0x40e00000, v20
	v_mul_f32_e32 v22, v22, v36
	v_mul_f32_e32 v36, 0xc01d265f, v20
	v_mul_f32_e32 v22, v30, v22
	v_add_f32_e32 v30, 1.0, v37
	v_rcp_f32_e32 v30, v30
	v_exp_f32_e32 v36, v36
	v_med3_f32 v31, v31, s60, v239
	v_min_f32_e32 v21, 0x40e00000, v21
	v_mul_f32_e32 v23, v23, v30
	v_mov_b32_e32 v30, v31
	v_add_f32_e32 v31, 1.0, v36
	v_mul_f32_e32 v36, 0xc01d265f, v21
	v_exp_f32_e32 v36, v36
	v_rcp_f32_e32 v31, v31
	v_pk_fma_f32 v[28:29], v[110:111], s[26:27], v[16:17] op_sel_hi:[1,0,1]
	v_mul_f32_e32 v23, v30, v23
	v_add_f32_e32 v30, 1.0, v36
	v_pk_fma_f32 v[26:27], v[112:113], s[26:27], v[6:7] op_sel_hi:[1,0,1]
	v_med3_f32 v28, v28, s60, v239
	v_rcp_f32_e32 v30, v30
	v_mul_f32_e32 v20, v20, v31
	v_min_f32_e32 v26, 0x40e00000, v26
	v_mul_f32_e32 v28, v28, v20
	v_med3_f32 v20, v29, s60, v239
	v_mul_f32_e32 v29, 0xc01d265f, v26
	v_mul_f32_e32 v21, v21, v30
	v_exp_f32_e32 v29, v29
	v_mul_f32_e32 v21, v20, v21
	v_mov_b32_e32 v20, v67
	v_cvt_pk_fp8_f32 v20, v22, v23
	v_min_f32_e32 v23, 0x40e00000, v27
	v_mul_f32_e32 v27, 0xc01d265f, v23
	v_add_f32_e32 v22, 1.0, v29
	v_rcp_f32_e32 v22, v22
	v_exp_f32_e32 v27, v27
	v_pk_fma_f32 v[24:25], v[114:115], s[26:27], v[8:9] op_sel_hi:[1,0,1]
	v_pk_fma_f32 v[34:35], v[104:105], s[26:27], v[2:3] op_sel_hi:[1,0,1]
	v_mul_f32_e32 v22, v26, v22
	v_add_f32_e32 v26, 1.0, v27
	v_rcp_f32_e32 v26, v26
	v_min_f32_e32 v24, 0x40e00000, v24
	v_min_f32_e32 v25, 0x40e00000, v25
	v_cvt_pk_fp8_f32 v20, v28, v21 op_sel:[0,0,1]
	v_mul_f32_e32 v23, v23, v26
	v_mul_f32_e32 v26, 0xc01d265f, v24
	v_exp_f32_e32 v26, v26
	v_med3_f32 v21, v34, s60, v239
	v_mul_f32_e32 v27, 0xc01d265f, v25
	v_add_f32_e32 v26, 1.0, v26
	v_rcp_f32_e32 v26, v26
	v_mul_f32_e32 v22, v21, v22
	v_med3_f32 v21, v35, s60, v239
	v_exp_f32_e32 v27, v27
	v_pk_fma_f32 v[32:33], v[106:107], s[26:27], v[4:5] op_sel_hi:[1,0,1]
	v_mul_f32_e32 v23, v21, v23
	v_med3_f32 v21, v32, s60, v239
	v_mul_f32_e32 v24, v24, v26
	v_mul_f32_e32 v24, v21, v24
	v_add_f32_e32 v21, 1.0, v27
	v_rcp_f32_e32 v26, v21
	v_mov_b32_e32 v21, v67
	v_cvt_pk_fp8_f32 v21, v22, v23
	v_med3_f32 v27, v33, s60, v239
	v_mul_f32_e32 v22, v25, v26
	v_mov_b32_e32 v23, v27
	v_mul_f32_e32 v22, v23, v22
	v_cvt_pk_fp8_f32 v21, v24, v22 op_sel:[0,0,1]
	v_add_co_u32_e32 v22, vcc, s62, v18
	v_pk_fma_f32 v[30:31], v[100:101], s[26:27], v[14:15] op_sel_hi:[1,0,1]
	s_nop 0
	v_addc_co_u32_e32 v23, vcc, 0, v19, vcc
	global_store_dwordx2 v[22:23], v[20:21], off
	v_pk_fma_f32 v[22:23], v[92:93], s[26:27], v[10:11] op_sel_hi:[1,0,1]
	v_pk_fma_f32 v[20:21], v[94:95], s[26:27], v[12:13] op_sel_hi:[1,0,1]
	v_min_f32_e32 v22, 0x40e00000, v22
	v_mul_f32_e32 v32, 0xc01d265f, v22
	v_exp_f32_e32 v36, v32
	v_min_f32_e32 v23, 0x40e00000, v23
	v_mul_f32_e32 v37, 0xc01d265f, v23
	v_add_f32_e32 v36, 1.0, v36
	v_rcp_f32_e32 v36, v36
	v_exp_f32_e32 v37, v37
	v_med3_f32 v30, v30, s60, v239
	v_min_f32_e32 v20, 0x40e00000, v20
	v_mul_f32_e32 v22, v22, v36
	v_mul_f32_e32 v36, 0xc01d265f, v20
	v_mul_f32_e32 v22, v30, v22
	v_add_f32_e32 v30, 1.0, v37
	v_rcp_f32_e32 v30, v30
	v_exp_f32_e32 v36, v36
	v_med3_f32 v31, v31, s60, v239
	v_min_f32_e32 v21, 0x40e00000, v21
	v_mul_f32_e32 v23, v23, v30
	v_mov_b32_e32 v30, v31
	v_add_f32_e32 v31, 1.0, v36
	v_mul_f32_e32 v36, 0xc01d265f, v21
	v_exp_f32_e32 v36, v36
	v_rcp_f32_e32 v31, v31
	v_pk_fma_f32 v[28:29], v[102:103], s[26:27], v[16:17] op_sel_hi:[1,0,1]
	v_mul_f32_e32 v23, v30, v23
	v_add_f32_e32 v30, 1.0, v36
	v_pk_fma_f32 v[26:27], v[88:89], s[26:27], v[6:7] op_sel_hi:[1,0,1]
	v_med3_f32 v28, v28, s60, v239
	v_rcp_f32_e32 v30, v30
	v_mul_f32_e32 v20, v20, v31
	v_min_f32_e32 v26, 0x40e00000, v26
	v_mul_f32_e32 v28, v28, v20
	v_med3_f32 v20, v29, s60, v239
	v_mul_f32_e32 v29, 0xc01d265f, v26
	v_mul_f32_e32 v21, v21, v30
	v_exp_f32_e32 v29, v29
	v_mul_f32_e32 v21, v20, v21
	v_mov_b32_e32 v20, v67
	v_cvt_pk_fp8_f32 v20, v22, v23
	v_min_f32_e32 v23, 0x40e00000, v27
	v_mul_f32_e32 v27, 0xc01d265f, v23
	v_add_f32_e32 v22, 1.0, v29
	v_rcp_f32_e32 v22, v22
	v_exp_f32_e32 v27, v27
	v_pk_fma_f32 v[24:25], v[90:91], s[26:27], v[8:9] op_sel_hi:[1,0,1]
	v_pk_fma_f32 v[34:35], v[96:97], s[26:27], v[2:3] op_sel_hi:[1,0,1]
	v_mul_f32_e32 v22, v26, v22
	v_add_f32_e32 v26, 1.0, v27
	v_rcp_f32_e32 v26, v26
	v_min_f32_e32 v24, 0x40e00000, v24
	v_min_f32_e32 v25, 0x40e00000, v25
	v_cvt_pk_fp8_f32 v20, v28, v21 op_sel:[0,0,1]
	v_mul_f32_e32 v23, v23, v26
	v_mul_f32_e32 v26, 0xc01d265f, v24
	v_exp_f32_e32 v26, v26
	v_med3_f32 v21, v34, s60, v239
	v_mul_f32_e32 v27, 0xc01d265f, v25
	v_add_f32_e32 v26, 1.0, v26
	v_rcp_f32_e32 v26, v26
	v_mul_f32_e32 v22, v21, v22
	v_med3_f32 v21, v35, s60, v239
	v_exp_f32_e32 v27, v27
	v_pk_fma_f32 v[32:33], v[98:99], s[26:27], v[4:5] op_sel_hi:[1,0,1]
	v_mul_f32_e32 v23, v21, v23
	v_med3_f32 v21, v32, s60, v239
	v_mul_f32_e32 v24, v24, v26
	v_mul_f32_e32 v24, v21, v24
	v_add_f32_e32 v21, 1.0, v27
	v_rcp_f32_e32 v26, v21
	v_mov_b32_e32 v21, v67
	v_cvt_pk_fp8_f32 v21, v22, v23
	v_med3_f32 v27, v33, s60, v239
	v_mul_f32_e32 v22, v25, v26
	v_mov_b32_e32 v23, v27
	v_mul_f32_e32 v22, v23, v22
	v_cvt_pk_fp8_f32 v21, v24, v22 op_sel:[0,0,1]
	v_add_co_u32_e32 v22, vcc, s63, v18
	v_pk_fma_f32 v[10:11], v[76:77], s[26:27], v[10:11] op_sel_hi:[1,0,1]
	s_nop 0
	v_addc_co_u32_e32 v23, vcc, 0, v19, vcc
	v_min_f32_e32 v10, 0x40e00000, v10
	global_store_dwordx2 v[22:23], v[20:21], off
	v_mul_f32_e32 v20, 0xc01d265f, v10
	v_exp_f32_e32 v20, v20
	v_min_f32_e32 v11, 0x40e00000, v11
	v_mul_f32_e32 v21, 0xc01d265f, v11
	v_add_f32_e32 v20, 1.0, v20
	v_rcp_f32_e32 v20, v20
	v_exp_f32_e32 v21, v21
	v_pk_fma_f32 v[12:13], v[78:79], s[26:27], v[12:13] op_sel_hi:[1,0,1]
	v_pk_fma_f32 v[14:15], v[84:85], s[26:27], v[14:15] op_sel_hi:[1,0,1]
	v_min_f32_e32 v12, 0x40e00000, v12
	v_med3_f32 v14, v14, s60, v239
	v_mul_f32_e32 v10, v10, v20
	v_mul_f32_e32 v20, 0xc01d265f, v12
	v_mul_f32_e32 v10, v14, v10
	v_add_f32_e32 v14, 1.0, v21
	v_rcp_f32_e32 v14, v14
	v_exp_f32_e32 v20, v20
	v_med3_f32 v15, v15, s60, v239
	v_min_f32_e32 v13, 0x40e00000, v13
	v_mul_f32_e32 v11, v11, v14
	v_mov_b32_e32 v14, v15
	v_add_f32_e32 v15, 1.0, v20
	v_mul_f32_e32 v20, 0xc01d265f, v13
	v_rcp_f32_e32 v15, v15
	v_exp_f32_e32 v20, v20
	v_pk_fma_f32 v[6:7], v[72:73], s[26:27], v[6:7] op_sel_hi:[1,0,1]
	v_pk_fma_f32 v[16:17], v[86:87], s[26:27], v[16:17] op_sel_hi:[1,0,1]
	v_mul_f32_e32 v12, v12, v15
	v_add_f32_e32 v15, 1.0, v20
	v_rcp_f32_e32 v15, v15
	v_mul_f32_e32 v11, v14, v11
	v_med3_f32 v14, v16, s60, v239
	v_min_f32_e32 v7, 0x40e00000, v7
	v_mul_f32_e32 v13, v13, v15
	v_min_f32_e32 v15, 0x40e00000, v6
	v_mul_f32_e32 v6, 0xc01d265f, v15
	v_exp_f32_e32 v16, v6
	v_mov_b32_e32 v6, v67
	v_cvt_pk_fp8_f32 v6, v10, v11
	v_mul_f32_e32 v11, 0xc01d265f, v7
	v_add_f32_e32 v10, 1.0, v16
	v_rcp_f32_e32 v10, v10
	v_exp_f32_e32 v11, v11
	v_pk_fma_f32 v[2:3], v[80:81], s[26:27], v[2:3] op_sel_hi:[1,0,1]
	v_pk_fma_f32 v[8:9], v[74:75], s[26:27], v[8:9] op_sel_hi:[1,0,1]
	v_med3_f32 v2, v2, s60, v239
	v_mul_f32_e32 v10, v15, v10
	v_min_f32_e32 v8, 0x40e00000, v8
	v_add_f32_e32 v11, 1.0, v11
	v_mul_f32_e32 v2, v2, v10
	v_mul_f32_e32 v10, 0xc01d265f, v8
	v_rcp_f32_e32 v11, v11
	v_exp_f32_e32 v10, v10
	v_med3_f32 v3, v3, s60, v239
	v_mul_f32_e32 v7, v7, v11
	v_min_f32_e32 v9, 0x40e00000, v9
	v_mul_f32_e32 v3, v3, v7
	v_add_f32_e32 v7, 1.0, v10
	v_mul_f32_e32 v10, 0xc01d265f, v9
	v_rcp_f32_e32 v7, v7
	v_exp_f32_e32 v10, v10
	v_pk_fma_f32 v[4:5], v[82:83], s[26:27], v[4:5] op_sel_hi:[1,0,1]
	v_mul_f32_e32 v7, v8, v7
	v_med3_f32 v4, v4, s60, v239
	v_mul_f32_e32 v4, v4, v7
	v_add_f32_e32 v7, 1.0, v10
	v_rcp_f32_e32 v8, v7
	v_mov_b32_e32 v7, v67
	v_cvt_pk_fp8_f32 v7, v2, v3
	v_mul_f32_e32 v12, v14, v12
	v_med3_f32 v14, v17, s60, v239
	v_med3_f32 v5, v5, s60, v239
	v_mul_f32_e32 v2, v9, v8
	v_mov_b32_e32 v3, v5
	v_mul_f32_e32 v13, v14, v13
	v_mul_f32_e32 v2, v3, v2
	v_cvt_pk_fp8_f32 v6, v12, v13 op_sel:[0,0,1]
	v_cvt_pk_fp8_f32 v7, v4, v2 op_sel:[0,0,1]
	v_add_co_u32_e32 v2, vcc, 0x58000, v18
	s_nop 1
	v_addc_co_u32_e32 v3, vcc, 0, v19, vcc
	global_store_dwordx2 v[2:3], v[6:7], off
	s_nop 7
	s_and_b64 vcc, exec, s[0:1]
	s_mov_b64 s[0:1], -1
	s_cbranch_vccnz .LBB0_934
	s_andn2_b64 vcc, exec, s[14:15]
	s_cbranch_vccnz .LBB0_933
	s_barrier
	s_branch .LBB0_933
